# speedup vs baseline: 1.0026x; 1.0026x over previous
.Lc0_next0:
	s_waitcnt lgkmcnt(6)
	v_pk_fma_f16 v6, v2, v120, v121 op_sel:[0,0,0] op_sel_hi:[1,0,0] neg_lo:[1,0,0] neg_hi:[1,0,0]
	v_pk_fma_f16 v7, v3, v120, v121 op_sel:[0,0,0] op_sel_hi:[1,0,0] neg_lo:[1,0,0] neg_hi:[1,0,0]
	v_pk_fma_f16 v8, v4, v120, v121 op_sel:[0,0,0] op_sel_hi:[1,0,0] neg_lo:[1,0,0] neg_hi:[1,0,0]
	v_pk_fma_f16 v9, v5, v120, v121 op_sel:[0,0,0] op_sel_hi:[1,0,0] neg_lo:[1,0,0] neg_hi:[1,0,0]
	v_mfma_f32_16x16x32_f16 v[18:21], v[14:17], v[2:5], 0
	ds_read2_b64 v[72:75], v32 offset0:22 offset1:224
	ds_read_b128 v[132:135], v33 offset:176
	ds_read_b32 v37, v36 offset:8
	ds_read_b32 v38, v36 offset:72
	v_pk_fma_f16 v2, v48, v6, v2
	v_pk_fma_f16 v3, v49, v7, v3
	v_pk_fma_f16 v4, v50, v8, v4
	v_pk_fma_f16 v5, v51, v9, v5
	v_cndmask_b32_e64 v29, v29, v25, s[66:67]
	v_cvt_pk_f16_f32 v30, v26, v27
	v_cvt_pk_f16_f32 v31, v28, v29
	ds_write_b16 v39, v30 offset:2048
	ds_write_b16_d16_hi v39, v30 offset:2112
	ds_write_b16 v39, v31 offset:2176
	ds_write_b16_d16_hi v39, v31 offset:2240
	s_mov_b64 exec, 1
	ds_add_u32 v36, v44 offset:128
	s_mov_b64 exec, -1
	v_pk_fma_f16 v6, v2, v122, v123 op_sel:[0,0,0] op_sel_hi:[1,0,0] neg_lo:[1,0,0] neg_hi:[1,0,0]
	v_pk_fma_f16 v7, v3, v122, v123 op_sel:[0,0,0] op_sel_hi:[1,0,0] neg_lo:[1,0,0] neg_hi:[1,0,0]
	v_pk_fma_f16 v8, v4, v122, v123 op_sel:[0,0,0] op_sel_hi:[1,0,0] neg_lo:[1,0,0] neg_hi:[1,0,0]
	v_pk_fma_f16 v9, v5, v122, v123 op_sel:[0,0,0] op_sel_hi:[1,0,0] neg_lo:[1,0,0] neg_hi:[1,0,0]
	v_mfma_f32_16x16x32_f16 v[22:25], v[14:17], v[2:5], 0
	ds_read2_b64 v[76:79], v32 offset0:23 offset1:225
	v_pk_fma_f16 v2, v52, v6, v2
	v_pk_fma_f16 v3, v53, v7, v3
	v_pk_fma_f16 v4, v54, v8, v4
	v_pk_fma_f16 v5, v55, v9, v5
	v_cndmask_b32_e64 v26, v26, v18, s[60:61]
	s_waitcnt lgkmcnt(13)
	v_pk_fma_f16 v6, v2, v124, v125 op_sel:[0,0,0] op_sel_hi:[1,0,0] neg_lo:[1,0,0] neg_hi:[1,0,0]
	v_pk_fma_f16 v7, v3, v124, v125 op_sel:[0,0,0] op_sel_hi:[1,0,0] neg_lo:[1,0,0] neg_hi:[1,0,0]
	v_pk_fma_f16 v8, v4, v124, v125 op_sel:[0,0,0] op_sel_hi:[1,0,0] neg_lo:[1,0,0] neg_hi:[1,0,0]
	v_pk_fma_f16 v9, v5, v124, v125 op_sel:[0,0,0] op_sel_hi:[1,0,0] neg_lo:[1,0,0] neg_hi:[1,0,0]
	v_mfma_f32_16x16x32_f16 v[18:21], v[14:17], v[2:5], 0
	ds_read2_b64 v[80:83], v32 offset0:24 offset1:226
	ds_read_b128 v[136:139], v33 offset:192
	v_pk_fma_f16 v2, v56, v6, v2
	v_pk_fma_f16 v3, v57, v7, v3
	v_pk_fma_f16 v4, v58, v8, v4
	v_pk_fma_f16 v5, v59, v9, v5
	v_cndmask_b32_e64 v27, v27, v23, s[60:61]
	v_pk_fma_f16 v6, v2, v126, v127 op_sel:[0,0,0] op_sel_hi:[1,0,0] neg_lo:[1,0,0] neg_hi:[1,0,0]
	v_pk_fma_f16 v7, v3, v126, v127 op_sel:[0,0,0] op_sel_hi:[1,0,0] neg_lo:[1,0,0] neg_hi:[1,0,0]
	v_pk_fma_f16 v8, v4, v126, v127 op_sel:[0,0,0] op_sel_hi:[1,0,0] neg_lo:[1,0,0] neg_hi:[1,0,0]
	v_pk_fma_f16 v9, v5, v126, v127 op_sel:[0,0,0] op_sel_hi:[1,0,0] neg_lo:[1,0,0] neg_hi:[1,0,0]
	v_mfma_f32_16x16x32_f16 v[22:25], v[14:17], v[2:5], 0
	ds_read2_b64 v[84:87], v32 offset0:25 offset1:227
	v_pk_fma_f16 v2, v60, v6, v2
	v_pk_fma_f16 v3, v61, v7, v3
	v_pk_fma_f16 v4, v62, v8, v4
	v_pk_fma_f16 v5, v63, v9, v5
	v_cndmask_b32_e64 v28, v28, v20, s[60:61]
	s_waitcnt lgkmcnt(13)
	v_pk_fma_f16 v6, v2, v128, v129 op_sel:[0,0,0] op_sel_hi:[1,0,0] neg_lo:[1,0,0] neg_hi:[1,0,0]
	v_pk_fma_f16 v7, v3, v128, v129 op_sel:[0,0,0] op_sel_hi:[1,0,0] neg_lo:[1,0,0] neg_hi:[1,0,0]
	v_pk_fma_f16 v8, v4, v128, v129 op_sel:[0,0,0] op_sel_hi:[1,0,0] neg_lo:[1,0,0] neg_hi:[1,0,0]
	v_pk_fma_f16 v9, v5, v128, v129 op_sel:[0,0,0] op_sel_hi:[1,0,0] neg_lo:[1,0,0] neg_hi:[1,0,0]
	v_mfma_f32_16x16x32_f16 v[18:21], v[14:17], v[2:5], 0
	ds_read2_b64 v[88:91], v32 offset0:26 offset1:228
	ds_read_b128 v[140:143], v33 offset:208
	v_pk_fma_f16 v2, v64, v6, v2
	v_pk_fma_f16 v3, v65, v7, v3
	v_pk_fma_f16 v4, v66, v8, v4
	v_pk_fma_f16 v5, v67, v9, v5
	v_cndmask_b32_e64 v29, v29, v25, s[60:61]
	v_pk_fma_f16 v6, v2, v130, v131 op_sel:[0,0,0] op_sel_hi:[1,0,0] neg_lo:[1,0,0] neg_hi:[1,0,0]
	v_pk_fma_f16 v7, v3, v130, v131 op_sel:[0,0,0] op_sel_hi:[1,0,0] neg_lo:[1,0,0] neg_hi:[1,0,0]
	v_pk_fma_f16 v8, v4, v130, v131 op_sel:[0,0,0] op_sel_hi:[1,0,0] neg_lo:[1,0,0] neg_hi:[1,0,0]
	v_pk_fma_f16 v9, v5, v130, v131 op_sel:[0,0,0] op_sel_hi:[1,0,0] neg_lo:[1,0,0] neg_hi:[1,0,0]
	v_mfma_f32_16x16x32_f16 v[22:25], v[14:17], v[2:5], 0
	ds_read2_b64 v[92:95], v32 offset0:27 offset1:229
	v_pk_fma_f16 v2, v68, v6, v2
	v_pk_fma_f16 v3, v69, v7, v3
	v_pk_fma_f16 v4, v70, v8, v4
	v_pk_fma_f16 v5, v71, v9, v5
	v_cndmask_b32_e64 v26, v26, v18, s[62:63]
	s_waitcnt lgkmcnt(6)
	v_pk_fma_f16 v6, v2, v132, v133 op_sel:[0,0,0] op_sel_hi:[1,0,0] neg_lo:[1,0,0] neg_hi:[1,0,0]
	v_pk_fma_f16 v7, v3, v132, v133 op_sel:[0,0,0] op_sel_hi:[1,0,0] neg_lo:[1,0,0] neg_hi:[1,0,0]
	v_pk_fma_f16 v8, v4, v132, v133 op_sel:[0,0,0] op_sel_hi:[1,0,0] neg_lo:[1,0,0] neg_hi:[1,0,0]
	v_pk_fma_f16 v9, v5, v132, v133 op_sel:[0,0,0] op_sel_hi:[1,0,0] neg_lo:[1,0,0] neg_hi:[1,0,0]
	v_mfma_f32_16x16x32_f16 v[18:21], v[14:17], v[2:5], 0
	ds_read2_b64 v[96:99], v32 offset0:28 offset1:230
	ds_read_b128 v[144:147], v33 offset:224
	v_pk_fma_f16 v2, v72, v6, v2
	v_pk_fma_f16 v3, v73, v7, v3
	v_pk_fma_f16 v4, v74, v8, v4
	v_pk_fma_f16 v5, v75, v9, v5
	v_cndmask_b32_e64 v27, v27, v23, s[62:63]
	v_pk_fma_f16 v6, v2, v134, v135 op_sel:[0,0,0] op_sel_hi:[1,0,0] neg_lo:[1,0,0] neg_hi:[1,0,0]
	v_pk_fma_f16 v7, v3, v134, v135 op_sel:[0,0,0] op_sel_hi:[1,0,0] neg_lo:[1,0,0] neg_hi:[1,0,0]
	v_pk_fma_f16 v8, v4, v134, v135 op_sel:[0,0,0] op_sel_hi:[1,0,0] neg_lo:[1,0,0] neg_hi:[1,0,0]
	v_pk_fma_f16 v9, v5, v134, v135 op_sel:[0,0,0] op_sel_hi:[1,0,0] neg_lo:[1,0,0] neg_hi:[1,0,0]
	v_mfma_f32_16x16x32_f16 v[22:25], v[14:17], v[2:5], 0
	ds_read2_b64 v[100:103], v32 offset0:29 offset1:231
	v_pk_fma_f16 v2, v76, v6, v2
	v_pk_fma_f16 v3, v77, v7, v3
	v_pk_fma_f16 v4, v78, v8, v4
	v_pk_fma_f16 v5, v79, v9, v5
	v_cndmask_b32_e64 v28, v28, v20, s[62:63]
	s_waitcnt lgkmcnt(6)
	v_pk_fma_f16 v6, v2, v136, v137 op_sel:[0,0,0] op_sel_hi:[1,0,0] neg_lo:[1,0,0] neg_hi:[1,0,0]
	v_pk_fma_f16 v7, v3, v136, v137 op_sel:[0,0,0] op_sel_hi:[1,0,0] neg_lo:[1,0,0] neg_hi:[1,0,0]
	v_pk_fma_f16 v8, v4, v136, v137 op_sel:[0,0,0] op_sel_hi:[1,0,0] neg_lo:[1,0,0] neg_hi:[1,0,0]
	v_pk_fma_f16 v9, v5, v136, v137 op_sel:[0,0,0] op_sel_hi:[1,0,0] neg_lo:[1,0,0] neg_hi:[1,0,0]
	v_mfma_f32_16x16x32_f16 v[18:21], v[14:17], v[2:5], 0
	ds_read2_b64 v[104:107], v32 offset0:30 offset1:232
	ds_read_b128 v[148:151], v33 offset:240
	v_pk_fma_f16 v2, v80, v6, v2
	v_pk_fma_f16 v3, v81, v7, v3
	v_pk_fma_f16 v4, v82, v8, v4
	v_pk_fma_f16 v5, v83, v9, v5
	v_cndmask_b32_e64 v29, v29, v25, s[62:63]
	v_readfirstlane_b32 s4, v37
	v_readfirstlane_b32 s5, v38
	s_and_b32 s4, s4, s5
	s_cbranch_scc0 .Lc0_alt1

.Lc0_next1:
	v_add_u32_e32 v32, 0x100, v32
	v_add_u32_e32 v33, 0x100, v33
	v_add_u32_e32 v34, 0x100, v34
	v_add_u32_e32 v36, 8, v36
	v_add_u32_e32 v39, 0x1000, v39
	v_add_u32_e32 v43, 0x1000, v43
	v_add_u32_e32 v35, 0x800, v35
	s_xor_b32 s71, s71, 2
	s_add_i32 s70, s70, 1
	s_cmp_lt_u32 s70, 6
	s_cbranch_scc1 .Lc0_loop
	s_waitcnt lgkmcnt(6)
	v_pk_fma_f16 v6, v2, v120, v121 op_sel:[0,0,0] op_sel_hi:[1,0,0] neg_lo:[1,0,0] neg_hi:[1,0,0]
	v_pk_fma_f16 v7, v3, v120, v121 op_sel:[0,0,0] op_sel_hi:[1,0,0] neg_lo:[1,0,0] neg_hi:[1,0,0]
	v_pk_fma_f16 v8, v4, v120, v121 op_sel:[0,0,0] op_sel_hi:[1,0,0] neg_lo:[1,0,0] neg_hi:[1,0,0]
	v_pk_fma_f16 v9, v5, v120, v121 op_sel:[0,0,0] op_sel_hi:[1,0,0] neg_lo:[1,0,0] neg_hi:[1,0,0]
	v_mfma_f32_16x16x32_f16 v[18:21], v[10:13], v[2:5], 0
	ds_read2_b64 v[72:75], v32 offset0:6 offset1:208
	ds_read_b128 v[132:135], v33 offset:48
	v_pk_fma_f16 v2, v48, v6, v2
	v_pk_fma_f16 v3, v49, v7, v3
	v_pk_fma_f16 v4, v50, v8, v4
	v_pk_fma_f16 v5, v51, v9, v5
	v_cndmask_b32_e64 v29, v29, v25, s[66:67]
	v_cvt_pk_f16_f32 v30, v26, v27
	v_cvt_pk_f16_f32 v31, v28, v29
	ds_write_b16 v39, v30 offset:0
	ds_write_b16_d16_hi v39, v30 offset:64
	ds_write_b16 v39, v31 offset:128
	ds_write_b16_d16_hi v39, v31 offset:192
	s_mov_b64 exec, 1
	ds_add_u32 v36, v44 offset:124
	s_mov_b64 exec, -1
	v_pk_fma_f16 v6, v2, v122, v123 op_sel:[0,0,0] op_sel_hi:[1,0,0] neg_lo:[1,0,0] neg_hi:[1,0,0]
	v_pk_fma_f16 v7, v3, v122, v123 op_sel:[0,0,0] op_sel_hi:[1,0,0] neg_lo:[1,0,0] neg_hi:[1,0,0]
	v_pk_fma_f16 v8, v4, v122, v123 op_sel:[0,0,0] op_sel_hi:[1,0,0] neg_lo:[1,0,0] neg_hi:[1,0,0]
	v_pk_fma_f16 v9, v5, v122, v123 op_sel:[0,0,0] op_sel_hi:[1,0,0] neg_lo:[1,0,0] neg_hi:[1,0,0]
	v_mfma_f32_16x16x32_f16 v[22:25], v[10:13], v[2:5], 0
	ds_read2_b64 v[76:79], v32 offset0:7 offset1:209
	v_pk_fma_f16 v2, v52, v6, v2
	v_pk_fma_f16 v3, v53, v7, v3
	v_pk_fma_f16 v4, v54, v8, v4
	v_pk_fma_f16 v5, v55, v9, v5
	v_cndmask_b32_e64 v26, v26, v18, s[60:61]
	s_waitcnt lgkmcnt(11)
	v_pk_fma_f16 v6, v2, v124, v125 op_sel:[0,0,0] op_sel_hi:[1,0,0] neg_lo:[1,0,0] neg_hi:[1,0,0]
	v_pk_fma_f16 v7, v3, v124, v125 op_sel:[0,0,0] op_sel_hi:[1,0,0] neg_lo:[1,0,0] neg_hi:[1,0,0]
	v_pk_fma_f16 v8, v4, v124, v125 op_sel:[0,0,0] op_sel_hi:[1,0,0] neg_lo:[1,0,0] neg_hi:[1,0,0]
	v_pk_fma_f16 v9, v5, v124, v125 op_sel:[0,0,0] op_sel_hi:[1,0,0] neg_lo:[1,0,0] neg_hi:[1,0,0]
	v_mfma_f32_16x16x32_f16 v[18:21], v[10:13], v[2:5], 0
	v_pk_fma_f16 v2, v56, v6, v2
	v_pk_fma_f16 v3, v57, v7, v3
	v_pk_fma_f16 v4, v58, v8, v4
	v_pk_fma_f16 v5, v59, v9, v5
	v_cndmask_b32_e64 v27, v27, v23, s[60:61]
	v_pk_fma_f16 v6, v2, v126, v127 op_sel:[0,0,0] op_sel_hi:[1,0,0] neg_lo:[1,0,0] neg_hi:[1,0,0]
	v_pk_fma_f16 v7, v3, v126, v127 op_sel:[0,0,0] op_sel_hi:[1,0,0] neg_lo:[1,0,0] neg_hi:[1,0,0]
	v_pk_fma_f16 v8, v4, v126, v127 op_sel:[0,0,0] op_sel_hi:[1,0,0] neg_lo:[1,0,0] neg_hi:[1,0,0]
	v_pk_fma_f16 v9, v5, v126, v127 op_sel:[0,0,0] op_sel_hi:[1,0,0] neg_lo:[1,0,0] neg_hi:[1,0,0]
	v_mfma_f32_16x16x32_f16 v[22:25], v[10:13], v[2:5], 0
	v_pk_fma_f16 v2, v60, v6, v2
	v_pk_fma_f16 v3, v61, v7, v3
	v_pk_fma_f16 v4, v62, v8, v4
	v_pk_fma_f16 v5, v63, v9, v5
	v_cndmask_b32_e64 v28, v28, v20, s[60:61]
	s_waitcnt lgkmcnt(8)
	s_mov_b32 s72, 0
	s_cmp_eq_u32 s70, 0
	s_cbranch_scc1 .Lc0_ndt
	s_sub_i32 s4, 3, s71
	s_cmp_eq_u32 s36, s4
	s_cbranch_scc0 .Lc0_ndt
	s_mov_b32 s72, 1
	ds_read_b32 v45, v36 offset:124
	ds_read_b128 v[112:115], v43 offset:0
	ds_read_b128 v[116:119], v43 offset:1024

.Lc0_dgot:
	ds_read_b128 v[112:115], v43 offset:0
	ds_read_b128 v[116:119], v43 offset:1024
	s_waitcnt lgkmcnt(0)
	s_branch .Lc0_dbackt
.Lc0_alt0:
	s_mov_b32 s72, 0
	s_cmp_eq_u32 s70, 0
	s_cbranch_scc1 .Lc0_nda0
	s_sub_i32 s4, 3, s71
	s_cmp_eq_u32 s36, s4
	s_cbranch_scc0 .Lc0_nda0
	s_mov_b32 s72, 1
	ds_read_b32 v45, v36 offset:124
	ds_read_b128 v[112:115], v43 offset:0
	ds_read_b128 v[116:119], v43 offset:1024
.Lc0_nda0:
	v_pk_fma_f16 v6, v2, v138, v139 op_sel:[0,0,0] op_sel_hi:[1,0,0] neg_lo:[1,0,0] neg_hi:[1,0,0]
	v_pk_fma_f16 v7, v3, v138, v139 op_sel:[0,0,0] op_sel_hi:[1,0,0] neg_lo:[1,0,0] neg_hi:[1,0,0]
	v_pk_fma_f16 v8, v4, v138, v139 op_sel:[0,0,0] op_sel_hi:[1,0,0] neg_lo:[1,0,0] neg_hi:[1,0,0]
	v_pk_fma_f16 v9, v5, v138, v139 op_sel:[0,0,0] op_sel_hi:[1,0,0] neg_lo:[1,0,0] neg_hi:[1,0,0]
	v_mfma_f32_16x16x32_f16 v[22:25], v[10:13], v[2:5], 0
	ds_read2_b64 v[108:111], v32 offset0:15 offset1:217
	v_pk_fma_f16 v2, v84, v6, v2
	v_pk_fma_f16 v3, v85, v7, v3
	v_pk_fma_f16 v4, v86, v8, v4
	v_pk_fma_f16 v5, v87, v9, v5
	v_cndmask_b32_e64 v26, v26, v18, s[64:65]
	s_waitcnt lgkmcnt(0)
	v_pk_fma_f16 v6, v2, v140, v141 op_sel:[0,0,0] op_sel_hi:[1,0,0] neg_lo:[1,0,0] neg_hi:[1,0,0]
	v_pk_fma_f16 v7, v3, v140, v141 op_sel:[0,0,0] op_sel_hi:[1,0,0] neg_lo:[1,0,0] neg_hi:[1,0,0]
	v_pk_fma_f16 v8, v4, v140, v141 op_sel:[0,0,0] op_sel_hi:[1,0,0] neg_lo:[1,0,0] neg_hi:[1,0,0]
	v_pk_fma_f16 v9, v5, v140, v141 op_sel:[0,0,0] op_sel_hi:[1,0,0] neg_lo:[1,0,0] neg_hi:[1,0,0]
	v_mfma_f32_16x16x32_f16 v[18:21], v[10:13], v[2:5], 0
	v_pk_fma_f16 v2, v88, v6, v2
	v_pk_fma_f16 v3, v89, v7, v3
	v_pk_fma_f16 v4, v90, v8, v4
	v_pk_fma_f16 v5, v91, v9, v5
	v_cndmask_b32_e64 v27, v27, v23, s[64:65]
	v_pk_fma_f16 v6, v2, v142, v143 op_sel:[0,0,0] op_sel_hi:[1,0,0] neg_lo:[1,0,0] neg_hi:[1,0,0]
	v_pk_fma_f16 v7, v3, v142, v143 op_sel:[0,0,0] op_sel_hi:[1,0,0] neg_lo:[1,0,0] neg_hi:[1,0,0]
	v_pk_fma_f16 v8, v4, v142, v143 op_sel:[0,0,0] op_sel_hi:[1,0,0] neg_lo:[1,0,0] neg_hi:[1,0,0]
	v_pk_fma_f16 v9, v5, v142, v143 op_sel:[0,0,0] op_sel_hi:[1,0,0] neg_lo:[1,0,0] neg_hi:[1,0,0]
	v_mfma_f32_16x16x32_f16 v[22:25], v[10:13], v[2:5], 0
	v_pk_fma_f16 v2, v92, v6, v2
	v_pk_fma_f16 v3, v93, v7, v3
	v_pk_fma_f16 v4, v94, v8, v4
	v_pk_fma_f16 v5, v95, v9, v5
	v_cndmask_b32_e64 v28, v28, v20, s[64:65]
	v_pk_fma_f16 v6, v2, v144, v145 op_sel:[0,0,0] op_sel_hi:[1,0,0] neg_lo:[1,0,0] neg_hi:[1,0,0]
	v_pk_fma_f16 v7, v3, v144, v145 op_sel:[0,0,0] op_sel_hi:[1,0,0] neg_lo:[1,0,0] neg_hi:[1,0,0]
	v_pk_fma_f16 v8, v4, v144, v145 op_sel:[0,0,0] op_sel_hi:[1,0,0] neg_lo:[1,0,0] neg_hi:[1,0,0]
	v_pk_fma_f16 v9, v5, v144, v145 op_sel:[0,0,0] op_sel_hi:[1,0,0] neg_lo:[1,0,0] neg_hi:[1,0,0]
	v_mfma_f32_16x16x32_f16 v[18:21], v[10:13], v[2:5], 0
	v_pk_fma_f16 v2, v96, v6, v2
	v_pk_fma_f16 v3, v97, v7, v3
	v_pk_fma_f16 v4, v98, v8, v4
	v_pk_fma_f16 v5, v99, v9, v5
	v_cndmask_b32_e64 v29, v29, v25, s[64:65]
	s_cmp_eq_u32 s72, 1
	s_cbranch_scc0 .Lc0_nsa0
	s_waitcnt lgkmcnt(1)
	v_readfirstlane_b32 s4, v45
	s_cmp_eq_u32 s4, 4
	s_cbranch_scc0 .Lc0_dslowa0

.Lc0_nsa0:
	v_pk_fma_f16 v6, v2, v146, v147 op_sel:[0,0,0] op_sel_hi:[1,0,0] neg_lo:[1,0,0] neg_hi:[1,0,0]
	v_pk_fma_f16 v7, v3, v146, v147 op_sel:[0,0,0] op_sel_hi:[1,0,0] neg_lo:[1,0,0] neg_hi:[1,0,0]
	v_pk_fma_f16 v8, v4, v146, v147 op_sel:[0,0,0] op_sel_hi:[1,0,0] neg_lo:[1,0,0] neg_hi:[1,0,0]
	v_pk_fma_f16 v9, v5, v146, v147 op_sel:[0,0,0] op_sel_hi:[1,0,0] neg_lo:[1,0,0] neg_hi:[1,0,0]
	v_mfma_f32_16x16x32_f16 v[22:25], v[10:13], v[2:5], 0
	v_pk_fma_f16 v2, v100, v6, v2
	v_pk_fma_f16 v3, v101, v7, v3
	v_pk_fma_f16 v4, v102, v8, v4
	v_pk_fma_f16 v5, v103, v9, v5
	v_cndmask_b32_e64 v26, v26, v18, s[66:67]
	v_pk_fma_f16 v6, v2, v148, v149 op_sel:[0,0,0] op_sel_hi:[1,0,0] neg_lo:[1,0,0] neg_hi:[1,0,0]
	v_pk_fma_f16 v7, v3, v148, v149 op_sel:[0,0,0] op_sel_hi:[1,0,0] neg_lo:[1,0,0] neg_hi:[1,0,0]
	v_pk_fma_f16 v8, v4, v148, v149 op_sel:[0,0,0] op_sel_hi:[1,0,0] neg_lo:[1,0,0] neg_hi:[1,0,0]
	v_pk_fma_f16 v9, v5, v148, v149 op_sel:[0,0,0] op_sel_hi:[1,0,0] neg_lo:[1,0,0] neg_hi:[1,0,0]
	v_mfma_f32_16x16x32_f16 v[18:21], v[10:13], v[2:5], 0
	v_pk_fma_f16 v2, v104, v6, v2
	v_pk_fma_f16 v3, v105, v7, v3
	v_pk_fma_f16 v4, v106, v8, v4
	v_pk_fma_f16 v5, v107, v9, v5
	v_cndmask_b32_e64 v27, v27, v23, s[66:67]
	v_pk_fma_f16 v6, v2, v150, v151 op_sel:[0,0,0] op_sel_hi:[1,0,0] neg_lo:[1,0,0] neg_hi:[1,0,0]
	v_pk_fma_f16 v7, v3, v150, v151 op_sel:[0,0,0] op_sel_hi:[1,0,0] neg_lo:[1,0,0] neg_hi:[1,0,0]
	v_pk_fma_f16 v8, v4, v150, v151 op_sel:[0,0,0] op_sel_hi:[1,0,0] neg_lo:[1,0,0] neg_hi:[1,0,0]
	v_pk_fma_f16 v9, v5, v150, v151 op_sel:[0,0,0] op_sel_hi:[1,0,0] neg_lo:[1,0,0] neg_hi:[1,0,0]
	v_mfma_f32_16x16x32_f16 v[22:25], v[10:13], v[2:5], 0
	v_pk_fma_f16 v2, v108, v6, v2
	v_pk_fma_f16 v3, v109, v7, v3
	v_pk_fma_f16 v4, v110, v8, v4
	v_pk_fma_f16 v5, v111, v9, v5
	v_cndmask_b32_e64 v28, v28, v20, s[66:67]
.Lc0_aspin0:
	ds_read_b32 v37, v36 offset:4
	ds_read_b32 v38, v36 offset:68
	s_waitcnt lgkmcnt(0)
	v_readfirstlane_b32 s4, v37
	v_readfirstlane_b32 s5, v38
	s_and_b32 s4, s4, s5
	s_cbranch_scc1 .Lc0_ago0
	s_sleep 1
	s_add_i32 s73, s73, 1
	s_cmp_lt_u32 s73, 0x4000
	s_cbranch_scc1 .Lc0_aspin0
.Lc0_ago0:
	ds_read2_b64 v[48:51], v32 offset0:16 offset1:218
	ds_read_b128 v[120:123], v33 offset:128
	ds_read2_b64 v[14:17], v34 offset0:16 offset1:218
	ds_read2_b64 v[52:55], v32 offset0:17 offset1:219
	ds_read2_b64 v[56:59], v32 offset0:18 offset1:220
	ds_read_b128 v[124:127], v33 offset:144
	ds_read2_b64 v[60:63], v32 offset0:19 offset1:221
	ds_read2_b64 v[64:67], v32 offset0:20 offset1:222
	ds_read_b128 v[128:131], v33 offset:160
	ds_read2_b64 v[68:71], v32 offset0:21 offset1:223
	s_branch .Lc0_next0

.Lc0_dgoa0:
	ds_read_b128 v[112:115], v43 offset:0
	ds_read_b128 v[116:119], v43 offset:1024
	s_waitcnt lgkmcnt(0)
	s_branch .Lc0_dbacka0
.Lc0_alt1:
	s_mov_b32 s72, 0
	s_cmp_eq_u32 s36, s71
	s_cbranch_scc0 .Lc0_nda1
	s_mov_b32 s72, 1
	ds_read_b32 v45, v36 offset:128
	ds_read_b128 v[112:115], v43 offset:2048
	ds_read_b128 v[116:119], v43 offset:3072
.Lc0_nda1:
	v_pk_fma_f16 v6, v2, v138, v139 op_sel:[0,0,0] op_sel_hi:[1,0,0] neg_lo:[1,0,0] neg_hi:[1,0,0]
	v_pk_fma_f16 v7, v3, v138, v139 op_sel:[0,0,0] op_sel_hi:[1,0,0] neg_lo:[1,0,0] neg_hi:[1,0,0]
	v_pk_fma_f16 v8, v4, v138, v139 op_sel:[0,0,0] op_sel_hi:[1,0,0] neg_lo:[1,0,0] neg_hi:[1,0,0]
	v_pk_fma_f16 v9, v5, v138, v139 op_sel:[0,0,0] op_sel_hi:[1,0,0] neg_lo:[1,0,0] neg_hi:[1,0,0]
	v_mfma_f32_16x16x32_f16 v[22:25], v[14:17], v[2:5], 0
	ds_read2_b64 v[108:111], v32 offset0:31 offset1:233
	v_pk_fma_f16 v2, v84, v6, v2
	v_pk_fma_f16 v3, v85, v7, v3
	v_pk_fma_f16 v4, v86, v8, v4
	v_pk_fma_f16 v5, v87, v9, v5
	v_cndmask_b32_e64 v26, v26, v18, s[64:65]
	s_waitcnt lgkmcnt(0)
	v_pk_fma_f16 v6, v2, v140, v141 op_sel:[0,0,0] op_sel_hi:[1,0,0] neg_lo:[1,0,0] neg_hi:[1,0,0]
	v_pk_fma_f16 v7, v3, v140, v141 op_sel:[0,0,0] op_sel_hi:[1,0,0] neg_lo:[1,0,0] neg_hi:[1,0,0]
	v_pk_fma_f16 v8, v4, v140, v141 op_sel:[0,0,0] op_sel_hi:[1,0,0] neg_lo:[1,0,0] neg_hi:[1,0,0]
	v_pk_fma_f16 v9, v5, v140, v141 op_sel:[0,0,0] op_sel_hi:[1,0,0] neg_lo:[1,0,0] neg_hi:[1,0,0]
	v_mfma_f32_16x16x32_f16 v[18:21], v[14:17], v[2:5], 0
	v_pk_fma_f16 v2, v88, v6, v2
	v_pk_fma_f16 v3, v89, v7, v3
	v_pk_fma_f16 v4, v90, v8, v4
	v_pk_fma_f16 v5, v91, v9, v5
	v_cndmask_b32_e64 v27, v27, v23, s[64:65]
	v_pk_fma_f16 v6, v2, v142, v143 op_sel:[0,0,0] op_sel_hi:[1,0,0] neg_lo:[1,0,0] neg_hi:[1,0,0]
	v_pk_fma_f16 v7, v3, v142, v143 op_sel:[0,0,0] op_sel_hi:[1,0,0] neg_lo:[1,0,0] neg_hi:[1,0,0]
	v_pk_fma_f16 v8, v4, v142, v143 op_sel:[0,0,0] op_sel_hi:[1,0,0] neg_lo:[1,0,0] neg_hi:[1,0,0]
	v_pk_fma_f16 v9, v5, v142, v143 op_sel:[0,0,0] op_sel_hi:[1,0,0] neg_lo:[1,0,0] neg_hi:[1,0,0]
	v_mfma_f32_16x16x32_f16 v[22:25], v[14:17], v[2:5], 0
	v_pk_fma_f16 v2, v92, v6, v2
	v_pk_fma_f16 v3, v93, v7, v3
	v_pk_fma_f16 v4, v94, v8, v4
	v_pk_fma_f16 v5, v95, v9, v5
	v_cndmask_b32_e64 v28, v28, v20, s[64:65]
	v_pk_fma_f16 v6, v2, v144, v145 op_sel:[0,0,0] op_sel_hi:[1,0,0] neg_lo:[1,0,0] neg_hi:[1,0,0]
	v_pk_fma_f16 v7, v3, v144, v145 op_sel:[0,0,0] op_sel_hi:[1,0,0] neg_lo:[1,0,0] neg_hi:[1,0,0]
	v_pk_fma_f16 v8, v4, v144, v145 op_sel:[0,0,0] op_sel_hi:[1,0,0] neg_lo:[1,0,0] neg_hi:[1,0,0]
	v_pk_fma_f16 v9, v5, v144, v145 op_sel:[0,0,0] op_sel_hi:[1,0,0] neg_lo:[1,0,0] neg_hi:[1,0,0]
	v_mfma_f32_16x16x32_f16 v[18:21], v[14:17], v[2:5], 0
	v_pk_fma_f16 v2, v96, v6, v2
	v_pk_fma_f16 v3, v97, v7, v3
	v_pk_fma_f16 v4, v98, v8, v4
	v_pk_fma_f16 v5, v99, v9, v5
	v_cndmask_b32_e64 v29, v29, v25, s[64:65]
	s_cmp_eq_u32 s72, 1
	s_cbranch_scc0 .Lc0_nsa1
	s_waitcnt lgkmcnt(1)
	v_readfirstlane_b32 s4, v45
	s_cmp_eq_u32 s4, 4
	s_cbranch_scc0 .Lc0_dslowa1

.Lc0_nsa1:
	v_pk_fma_f16 v6, v2, v146, v147 op_sel:[0,0,0] op_sel_hi:[1,0,0] neg_lo:[1,0,0] neg_hi:[1,0,0]
	v_pk_fma_f16 v7, v3, v146, v147 op_sel:[0,0,0] op_sel_hi:[1,0,0] neg_lo:[1,0,0] neg_hi:[1,0,0]
	v_pk_fma_f16 v8, v4, v146, v147 op_sel:[0,0,0] op_sel_hi:[1,0,0] neg_lo:[1,0,0] neg_hi:[1,0,0]
	v_pk_fma_f16 v9, v5, v146, v147 op_sel:[0,0,0] op_sel_hi:[1,0,0] neg_lo:[1,0,0] neg_hi:[1,0,0]
	v_mfma_f32_16x16x32_f16 v[22:25], v[14:17], v[2:5], 0
	v_pk_fma_f16 v2, v100, v6, v2
	v_pk_fma_f16 v3, v101, v7, v3
	v_pk_fma_f16 v4, v102, v8, v4
	v_pk_fma_f16 v5, v103, v9, v5
	v_cndmask_b32_e64 v26, v26, v18, s[66:67]
	v_pk_fma_f16 v6, v2, v148, v149 op_sel:[0,0,0] op_sel_hi:[1,0,0] neg_lo:[1,0,0] neg_hi:[1,0,0]
	v_pk_fma_f16 v7, v3, v148, v149 op_sel:[0,0,0] op_sel_hi:[1,0,0] neg_lo:[1,0,0] neg_hi:[1,0,0]
	v_pk_fma_f16 v8, v4, v148, v149 op_sel:[0,0,0] op_sel_hi:[1,0,0] neg_lo:[1,0,0] neg_hi:[1,0,0]
	v_pk_fma_f16 v9, v5, v148, v149 op_sel:[0,0,0] op_sel_hi:[1,0,0] neg_lo:[1,0,0] neg_hi:[1,0,0]
	v_mfma_f32_16x16x32_f16 v[18:21], v[14:17], v[2:5], 0
	v_pk_fma_f16 v2, v104, v6, v2
	v_pk_fma_f16 v3, v105, v7, v3
	v_pk_fma_f16 v4, v106, v8, v4
	v_pk_fma_f16 v5, v107, v9, v5
	v_cndmask_b32_e64 v27, v27, v23, s[66:67]
	v_pk_fma_f16 v6, v2, v150, v151 op_sel:[0,0,0] op_sel_hi:[1,0,0] neg_lo:[1,0,0] neg_hi:[1,0,0]
	v_pk_fma_f16 v7, v3, v150, v151 op_sel:[0,0,0] op_sel_hi:[1,0,0] neg_lo:[1,0,0] neg_hi:[1,0,0]
	v_pk_fma_f16 v8, v4, v150, v151 op_sel:[0,0,0] op_sel_hi:[1,0,0] neg_lo:[1,0,0] neg_hi:[1,0,0]
	v_pk_fma_f16 v9, v5, v150, v151 op_sel:[0,0,0] op_sel_hi:[1,0,0] neg_lo:[1,0,0] neg_hi:[1,0,0]
	v_mfma_f32_16x16x32_f16 v[22:25], v[14:17], v[2:5], 0
	v_pk_fma_f16 v2, v108, v6, v2
	v_pk_fma_f16 v3, v109, v7, v3
	v_pk_fma_f16 v4, v110, v8, v4
	v_pk_fma_f16 v5, v111, v9, v5
	v_cndmask_b32_e64 v28, v28, v20, s[66:67]
.Lc0_aspin1:
	ds_read_b32 v37, v36 offset:8
	ds_read_b32 v38, v36 offset:72
	s_waitcnt lgkmcnt(0)
	v_readfirstlane_b32 s4, v37
	v_readfirstlane_b32 s5, v38
	s_and_b32 s4, s4, s5
	s_cbranch_scc1 .Lc0_ago1
	s_sleep 1
	s_add_i32 s73, s73, 1
	s_cmp_lt_u32 s73, 0x4000
	s_cbranch_scc1 .Lc0_aspin1
.Lc0_ago1:
	ds_read2_b64 v[48:51], v32 offset0:32 offset1:234
	ds_read_b128 v[120:123], v33 offset:256
	ds_read2_b64 v[10:13], v34 offset0:32 offset1:234
	ds_read2_b64 v[52:55], v32 offset0:33 offset1:235
	ds_read2_b64 v[56:59], v32 offset0:34 offset1:236
	ds_read_b128 v[124:127], v33 offset:272
	ds_read2_b64 v[60:63], v32 offset0:35 offset1:237
	ds_read2_b64 v[64:67], v32 offset0:36 offset1:238
	ds_read_b128 v[128:131], v33 offset:288
	ds_read2_b64 v[68:71], v32 offset0:37 offset1:239
	s_branch .Lc0_next1

.Lc0_dgoa1:
	ds_read_b128 v[112:115], v43 offset:2048
	ds_read_b128 v[116:119], v43 offset:3072
	s_waitcnt lgkmcnt(0)
	s_branch .Lc0_dbacka1
.Lc_par1:
	ds_read2_b64 v[48:51], v32 offset0:0 offset1:202
	ds_read_b128 v[120:123], v33 offset:0
	ds_read2_b64 v[10:13], v34 offset0:0 offset1:202
	ds_read2_b64 v[52:55], v32 offset0:1 offset1:203
	ds_read2_b64 v[56:59], v32 offset0:2 offset1:204
	ds_read_b128 v[124:127], v33 offset:16
	ds_read2_b64 v[60:63], v32 offset0:3 offset1:205
	ds_read2_b64 v[64:67], v32 offset0:4 offset1:206
	ds_read_b128 v[128:131], v33 offset:32
	ds_read2_b64 v[68:71], v32 offset0:5 offset1:207
	s_mov_b32 s70, 0
	s_mov_b32 s71, 0

.Lc1_next0:
	s_waitcnt lgkmcnt(6)
	v_pk_fma_f16 v6, v2, v120, v121 op_sel:[0,1,1] op_sel_hi:[1,1,1] neg_lo:[1,0,0] neg_hi:[1,0,0]
	v_pk_fma_f16 v7, v3, v120, v121 op_sel:[0,1,1] op_sel_hi:[1,1,1] neg_lo:[1,0,0] neg_hi:[1,0,0]
	v_pk_fma_f16 v8, v4, v120, v121 op_sel:[0,1,1] op_sel_hi:[1,1,1] neg_lo:[1,0,0] neg_hi:[1,0,0]
	v_pk_fma_f16 v9, v5, v120, v121 op_sel:[0,1,1] op_sel_hi:[1,1,1] neg_lo:[1,0,0] neg_hi:[1,0,0]
	v_mfma_f32_16x16x32_f16 v[18:21], v[14:17], v[2:5], 0
	ds_read2_b64 v[72:75], v32 offset0:22 offset1:224
	ds_read_b128 v[132:135], v33 offset:176
	ds_read_b32 v37, v36 offset:8
	ds_read_b32 v38, v36 offset:72
	v_pk_fma_f16 v2, v48, v6, v2
	v_pk_fma_f16 v3, v49, v7, v3
	v_pk_fma_f16 v4, v50, v8, v4
	v_pk_fma_f16 v5, v51, v9, v5
	v_cndmask_b32_e64 v29, v29, v25, s[66:67]
	v_cvt_pk_f16_f32 v30, v26, v27
	v_cvt_pk_f16_f32 v31, v28, v29
	ds_write_b16 v39, v30 offset:2048
	ds_write_b16_d16_hi v39, v30 offset:2112
	ds_write_b16 v39, v31 offset:2176
	ds_write_b16_d16_hi v39, v31 offset:2240
	s_mov_b64 exec, 1
	ds_add_u32 v36, v44 offset:128
	s_mov_b64 exec, -1
	v_pk_fma_f16 v6, v2, v122, v123 op_sel:[0,1,1] op_sel_hi:[1,1,1] neg_lo:[1,0,0] neg_hi:[1,0,0]
	v_pk_fma_f16 v7, v3, v122, v123 op_sel:[0,1,1] op_sel_hi:[1,1,1] neg_lo:[1,0,0] neg_hi:[1,0,0]
	v_pk_fma_f16 v8, v4, v122, v123 op_sel:[0,1,1] op_sel_hi:[1,1,1] neg_lo:[1,0,0] neg_hi:[1,0,0]
	v_pk_fma_f16 v9, v5, v122, v123 op_sel:[0,1,1] op_sel_hi:[1,1,1] neg_lo:[1,0,0] neg_hi:[1,0,0]
	v_mfma_f32_16x16x32_f16 v[22:25], v[14:17], v[2:5], 0
	ds_read2_b64 v[76:79], v32 offset0:23 offset1:225
	v_pk_fma_f16 v2, v52, v6, v2
	v_pk_fma_f16 v3, v53, v7, v3
	v_pk_fma_f16 v4, v54, v8, v4
	v_pk_fma_f16 v5, v55, v9, v5
	v_cndmask_b32_e64 v26, v26, v18, s[60:61]
	s_waitcnt lgkmcnt(13)
	v_pk_fma_f16 v6, v2, v124, v125 op_sel:[0,1,1] op_sel_hi:[1,1,1] neg_lo:[1,0,0] neg_hi:[1,0,0]
	v_pk_fma_f16 v7, v3, v124, v125 op_sel:[0,1,1] op_sel_hi:[1,1,1] neg_lo:[1,0,0] neg_hi:[1,0,0]
	v_pk_fma_f16 v8, v4, v124, v125 op_sel:[0,1,1] op_sel_hi:[1,1,1] neg_lo:[1,0,0] neg_hi:[1,0,0]
	v_pk_fma_f16 v9, v5, v124, v125 op_sel:[0,1,1] op_sel_hi:[1,1,1] neg_lo:[1,0,0] neg_hi:[1,0,0]
	v_mfma_f32_16x16x32_f16 v[18:21], v[14:17], v[2:5], 0
	ds_read2_b64 v[80:83], v32 offset0:24 offset1:226
	ds_read_b128 v[136:139], v33 offset:192
	v_pk_fma_f16 v2, v56, v6, v2
	v_pk_fma_f16 v3, v57, v7, v3
	v_pk_fma_f16 v4, v58, v8, v4
	v_pk_fma_f16 v5, v59, v9, v5
	v_cndmask_b32_e64 v27, v27, v23, s[60:61]
	v_pk_fma_f16 v6, v2, v126, v127 op_sel:[0,1,1] op_sel_hi:[1,1,1] neg_lo:[1,0,0] neg_hi:[1,0,0]
	v_pk_fma_f16 v7, v3, v126, v127 op_sel:[0,1,1] op_sel_hi:[1,1,1] neg_lo:[1,0,0] neg_hi:[1,0,0]
	v_pk_fma_f16 v8, v4, v126, v127 op_sel:[0,1,1] op_sel_hi:[1,1,1] neg_lo:[1,0,0] neg_hi:[1,0,0]
	v_pk_fma_f16 v9, v5, v126, v127 op_sel:[0,1,1] op_sel_hi:[1,1,1] neg_lo:[1,0,0] neg_hi:[1,0,0]
	v_mfma_f32_16x16x32_f16 v[22:25], v[14:17], v[2:5], 0
	ds_read2_b64 v[84:87], v32 offset0:25 offset1:227
	v_pk_fma_f16 v2, v60, v6, v2
	v_pk_fma_f16 v3, v61, v7, v3
	v_pk_fma_f16 v4, v62, v8, v4
	v_pk_fma_f16 v5, v63, v9, v5
	v_cndmask_b32_e64 v28, v28, v20, s[60:61]
	s_waitcnt lgkmcnt(13)
	v_pk_fma_f16 v6, v2, v128, v129 op_sel:[0,1,1] op_sel_hi:[1,1,1] neg_lo:[1,0,0] neg_hi:[1,0,0]
	v_pk_fma_f16 v7, v3, v128, v129 op_sel:[0,1,1] op_sel_hi:[1,1,1] neg_lo:[1,0,0] neg_hi:[1,0,0]
	v_pk_fma_f16 v8, v4, v128, v129 op_sel:[0,1,1] op_sel_hi:[1,1,1] neg_lo:[1,0,0] neg_hi:[1,0,0]
	v_pk_fma_f16 v9, v5, v128, v129 op_sel:[0,1,1] op_sel_hi:[1,1,1] neg_lo:[1,0,0] neg_hi:[1,0,0]
	v_mfma_f32_16x16x32_f16 v[18:21], v[14:17], v[2:5], 0
	ds_read2_b64 v[88:91], v32 offset0:26 offset1:228
	ds_read_b128 v[140:143], v33 offset:208
	v_pk_fma_f16 v2, v64, v6, v2
	v_pk_fma_f16 v3, v65, v7, v3
	v_pk_fma_f16 v4, v66, v8, v4
	v_pk_fma_f16 v5, v67, v9, v5
	v_cndmask_b32_e64 v29, v29, v25, s[60:61]
	v_pk_fma_f16 v6, v2, v130, v131 op_sel:[0,1,1] op_sel_hi:[1,1,1] neg_lo:[1,0,0] neg_hi:[1,0,0]
	v_pk_fma_f16 v7, v3, v130, v131 op_sel:[0,1,1] op_sel_hi:[1,1,1] neg_lo:[1,0,0] neg_hi:[1,0,0]
	v_pk_fma_f16 v8, v4, v130, v131 op_sel:[0,1,1] op_sel_hi:[1,1,1] neg_lo:[1,0,0] neg_hi:[1,0,0]
	v_pk_fma_f16 v9, v5, v130, v131 op_sel:[0,1,1] op_sel_hi:[1,1,1] neg_lo:[1,0,0] neg_hi:[1,0,0]
	v_mfma_f32_16x16x32_f16 v[22:25], v[14:17], v[2:5], 0
	ds_read2_b64 v[92:95], v32 offset0:27 offset1:229
	v_pk_fma_f16 v2, v68, v6, v2
	v_pk_fma_f16 v3, v69, v7, v3
	v_pk_fma_f16 v4, v70, v8, v4
	v_pk_fma_f16 v5, v71, v9, v5
	v_cndmask_b32_e64 v26, v26, v18, s[62:63]
	s_waitcnt lgkmcnt(6)
	v_pk_fma_f16 v6, v2, v132, v133 op_sel:[0,1,1] op_sel_hi:[1,1,1] neg_lo:[1,0,0] neg_hi:[1,0,0]
	v_pk_fma_f16 v7, v3, v132, v133 op_sel:[0,1,1] op_sel_hi:[1,1,1] neg_lo:[1,0,0] neg_hi:[1,0,0]
	v_pk_fma_f16 v8, v4, v132, v133 op_sel:[0,1,1] op_sel_hi:[1,1,1] neg_lo:[1,0,0] neg_hi:[1,0,0]
	v_pk_fma_f16 v9, v5, v132, v133 op_sel:[0,1,1] op_sel_hi:[1,1,1] neg_lo:[1,0,0] neg_hi:[1,0,0]
	v_mfma_f32_16x16x32_f16 v[18:21], v[14:17], v[2:5], 0
	ds_read2_b64 v[96:99], v32 offset0:28 offset1:230
	ds_read_b128 v[144:147], v33 offset:224
	v_pk_fma_f16 v2, v72, v6, v2
	v_pk_fma_f16 v3, v73, v7, v3
	v_pk_fma_f16 v4, v74, v8, v4
	v_pk_fma_f16 v5, v75, v9, v5
	v_cndmask_b32_e64 v27, v27, v23, s[62:63]
	v_pk_fma_f16 v6, v2, v134, v135 op_sel:[0,1,1] op_sel_hi:[1,1,1] neg_lo:[1,0,0] neg_hi:[1,0,0]
	v_pk_fma_f16 v7, v3, v134, v135 op_sel:[0,1,1] op_sel_hi:[1,1,1] neg_lo:[1,0,0] neg_hi:[1,0,0]
	v_pk_fma_f16 v8, v4, v134, v135 op_sel:[0,1,1] op_sel_hi:[1,1,1] neg_lo:[1,0,0] neg_hi:[1,0,0]
	v_pk_fma_f16 v9, v5, v134, v135 op_sel:[0,1,1] op_sel_hi:[1,1,1] neg_lo:[1,0,0] neg_hi:[1,0,0]
	v_mfma_f32_16x16x32_f16 v[22:25], v[14:17], v[2:5], 0
	ds_read2_b64 v[100:103], v32 offset0:29 offset1:231
	v_pk_fma_f16 v2, v76, v6, v2
	v_pk_fma_f16 v3, v77, v7, v3
	v_pk_fma_f16 v4, v78, v8, v4
	v_pk_fma_f16 v5, v79, v9, v5
	v_cndmask_b32_e64 v28, v28, v20, s[62:63]
	s_waitcnt lgkmcnt(6)
	v_pk_fma_f16 v6, v2, v136, v137 op_sel:[0,1,1] op_sel_hi:[1,1,1] neg_lo:[1,0,0] neg_hi:[1,0,0]
	v_pk_fma_f16 v7, v3, v136, v137 op_sel:[0,1,1] op_sel_hi:[1,1,1] neg_lo:[1,0,0] neg_hi:[1,0,0]
	v_pk_fma_f16 v8, v4, v136, v137 op_sel:[0,1,1] op_sel_hi:[1,1,1] neg_lo:[1,0,0] neg_hi:[1,0,0]
	v_pk_fma_f16 v9, v5, v136, v137 op_sel:[0,1,1] op_sel_hi:[1,1,1] neg_lo:[1,0,0] neg_hi:[1,0,0]
	v_mfma_f32_16x16x32_f16 v[18:21], v[14:17], v[2:5], 0
	ds_read2_b64 v[104:107], v32 offset0:30 offset1:232
	ds_read_b128 v[148:151], v33 offset:240
	v_pk_fma_f16 v2, v80, v6, v2
	v_pk_fma_f16 v3, v81, v7, v3
	v_pk_fma_f16 v4, v82, v8, v4
	v_pk_fma_f16 v5, v83, v9, v5
	v_cndmask_b32_e64 v29, v29, v25, s[62:63]
	v_readfirstlane_b32 s4, v37
	v_readfirstlane_b32 s5, v38
	s_and_b32 s4, s4, s5
	s_cbranch_scc0 .Lc1_alt1

.Lc1_next1:
	v_add_u32_e32 v32, 0x100, v32
	v_add_u32_e32 v33, 0x100, v33
	v_add_u32_e32 v34, 0x100, v34
	v_add_u32_e32 v36, 8, v36
	v_add_u32_e32 v39, 0x1000, v39
	v_add_u32_e32 v43, 0x1000, v43
	v_add_u32_e32 v35, 0x800, v35
	s_xor_b32 s71, s71, 2
	s_add_i32 s70, s70, 1
	s_cmp_lt_u32 s70, 6
	s_cbranch_scc1 .Lc1_loop
	s_waitcnt lgkmcnt(6)
	v_pk_fma_f16 v6, v2, v120, v121 op_sel:[0,1,1] op_sel_hi:[1,1,1] neg_lo:[1,0,0] neg_hi:[1,0,0]
	v_pk_fma_f16 v7, v3, v120, v121 op_sel:[0,1,1] op_sel_hi:[1,1,1] neg_lo:[1,0,0] neg_hi:[1,0,0]
	v_pk_fma_f16 v8, v4, v120, v121 op_sel:[0,1,1] op_sel_hi:[1,1,1] neg_lo:[1,0,0] neg_hi:[1,0,0]
	v_pk_fma_f16 v9, v5, v120, v121 op_sel:[0,1,1] op_sel_hi:[1,1,1] neg_lo:[1,0,0] neg_hi:[1,0,0]
	v_mfma_f32_16x16x32_f16 v[18:21], v[10:13], v[2:5], 0
	ds_read2_b64 v[72:75], v32 offset0:6 offset1:208
	ds_read_b128 v[132:135], v33 offset:48
	v_pk_fma_f16 v2, v48, v6, v2
	v_pk_fma_f16 v3, v49, v7, v3
	v_pk_fma_f16 v4, v50, v8, v4
	v_pk_fma_f16 v5, v51, v9, v5
	v_cndmask_b32_e64 v29, v29, v25, s[66:67]
	v_cvt_pk_f16_f32 v30, v26, v27
	v_cvt_pk_f16_f32 v31, v28, v29
	ds_write_b16 v39, v30 offset:0
	ds_write_b16_d16_hi v39, v30 offset:64
	ds_write_b16 v39, v31 offset:128
	ds_write_b16_d16_hi v39, v31 offset:192
	s_mov_b64 exec, 1
	ds_add_u32 v36, v44 offset:124
	s_mov_b64 exec, -1
	v_pk_fma_f16 v6, v2, v122, v123 op_sel:[0,1,1] op_sel_hi:[1,1,1] neg_lo:[1,0,0] neg_hi:[1,0,0]
	v_pk_fma_f16 v7, v3, v122, v123 op_sel:[0,1,1] op_sel_hi:[1,1,1] neg_lo:[1,0,0] neg_hi:[1,0,0]
	v_pk_fma_f16 v8, v4, v122, v123 op_sel:[0,1,1] op_sel_hi:[1,1,1] neg_lo:[1,0,0] neg_hi:[1,0,0]
	v_pk_fma_f16 v9, v5, v122, v123 op_sel:[0,1,1] op_sel_hi:[1,1,1] neg_lo:[1,0,0] neg_hi:[1,0,0]
	v_mfma_f32_16x16x32_f16 v[22:25], v[10:13], v[2:5], 0
	ds_read2_b64 v[76:79], v32 offset0:7 offset1:209
	v_pk_fma_f16 v2, v52, v6, v2
	v_pk_fma_f16 v3, v53, v7, v3
	v_pk_fma_f16 v4, v54, v8, v4
	v_pk_fma_f16 v5, v55, v9, v5
	v_cndmask_b32_e64 v26, v26, v18, s[60:61]
	s_waitcnt lgkmcnt(11)
	v_pk_fma_f16 v6, v2, v124, v125 op_sel:[0,1,1] op_sel_hi:[1,1,1] neg_lo:[1,0,0] neg_hi:[1,0,0]
	v_pk_fma_f16 v7, v3, v124, v125 op_sel:[0,1,1] op_sel_hi:[1,1,1] neg_lo:[1,0,0] neg_hi:[1,0,0]
	v_pk_fma_f16 v8, v4, v124, v125 op_sel:[0,1,1] op_sel_hi:[1,1,1] neg_lo:[1,0,0] neg_hi:[1,0,0]
	v_pk_fma_f16 v9, v5, v124, v125 op_sel:[0,1,1] op_sel_hi:[1,1,1] neg_lo:[1,0,0] neg_hi:[1,0,0]
	v_mfma_f32_16x16x32_f16 v[18:21], v[10:13], v[2:5], 0
	v_pk_fma_f16 v2, v56, v6, v2
	v_pk_fma_f16 v3, v57, v7, v3
	v_pk_fma_f16 v4, v58, v8, v4
	v_pk_fma_f16 v5, v59, v9, v5
	v_cndmask_b32_e64 v27, v27, v23, s[60:61]
	v_pk_fma_f16 v6, v2, v126, v127 op_sel:[0,1,1] op_sel_hi:[1,1,1] neg_lo:[1,0,0] neg_hi:[1,0,0]
	v_pk_fma_f16 v7, v3, v126, v127 op_sel:[0,1,1] op_sel_hi:[1,1,1] neg_lo:[1,0,0] neg_hi:[1,0,0]
	v_pk_fma_f16 v8, v4, v126, v127 op_sel:[0,1,1] op_sel_hi:[1,1,1] neg_lo:[1,0,0] neg_hi:[1,0,0]
	v_pk_fma_f16 v9, v5, v126, v127 op_sel:[0,1,1] op_sel_hi:[1,1,1] neg_lo:[1,0,0] neg_hi:[1,0,0]
	v_mfma_f32_16x16x32_f16 v[22:25], v[10:13], v[2:5], 0
	v_pk_fma_f16 v2, v60, v6, v2
	v_pk_fma_f16 v3, v61, v7, v3
	v_pk_fma_f16 v4, v62, v8, v4
	v_pk_fma_f16 v5, v63, v9, v5
	v_cndmask_b32_e64 v28, v28, v20, s[60:61]
	s_waitcnt lgkmcnt(8)
	s_mov_b32 s72, 0
	s_cmp_eq_u32 s70, 0
	s_cbranch_scc1 .Lc1_ndt
	s_sub_i32 s4, 3, s71
	s_cmp_eq_u32 s36, s4
	s_cbranch_scc0 .Lc1_ndt
	s_mov_b32 s72, 1
	ds_read_b32 v45, v36 offset:124
	ds_read_b128 v[112:115], v43 offset:0
	ds_read_b128 v[116:119], v43 offset:1024

.Lc1_dgot:
	ds_read_b128 v[112:115], v43 offset:0
	ds_read_b128 v[116:119], v43 offset:1024
	s_waitcnt lgkmcnt(0)
	s_branch .Lc1_dbackt
.Lc1_alt0:
	s_mov_b32 s72, 0
	s_cmp_eq_u32 s70, 0
	s_cbranch_scc1 .Lc1_nda0
	s_sub_i32 s4, 3, s71
	s_cmp_eq_u32 s36, s4
	s_cbranch_scc0 .Lc1_nda0
	s_mov_b32 s72, 1
	ds_read_b32 v45, v36 offset:124
	ds_read_b128 v[112:115], v43 offset:0
	ds_read_b128 v[116:119], v43 offset:1024
.Lc1_nda0:
	v_pk_fma_f16 v6, v2, v138, v139 op_sel:[0,1,1] op_sel_hi:[1,1,1] neg_lo:[1,0,0] neg_hi:[1,0,0]
	v_pk_fma_f16 v7, v3, v138, v139 op_sel:[0,1,1] op_sel_hi:[1,1,1] neg_lo:[1,0,0] neg_hi:[1,0,0]
	v_pk_fma_f16 v8, v4, v138, v139 op_sel:[0,1,1] op_sel_hi:[1,1,1] neg_lo:[1,0,0] neg_hi:[1,0,0]
	v_pk_fma_f16 v9, v5, v138, v139 op_sel:[0,1,1] op_sel_hi:[1,1,1] neg_lo:[1,0,0] neg_hi:[1,0,0]
	v_mfma_f32_16x16x32_f16 v[22:25], v[10:13], v[2:5], 0
	ds_read2_b64 v[108:111], v32 offset0:15 offset1:217
	v_pk_fma_f16 v2, v84, v6, v2
	v_pk_fma_f16 v3, v85, v7, v3
	v_pk_fma_f16 v4, v86, v8, v4
	v_pk_fma_f16 v5, v87, v9, v5
	v_cndmask_b32_e64 v26, v26, v18, s[64:65]
	s_waitcnt lgkmcnt(0)
	v_pk_fma_f16 v6, v2, v140, v141 op_sel:[0,1,1] op_sel_hi:[1,1,1] neg_lo:[1,0,0] neg_hi:[1,0,0]
	v_pk_fma_f16 v7, v3, v140, v141 op_sel:[0,1,1] op_sel_hi:[1,1,1] neg_lo:[1,0,0] neg_hi:[1,0,0]
	v_pk_fma_f16 v8, v4, v140, v141 op_sel:[0,1,1] op_sel_hi:[1,1,1] neg_lo:[1,0,0] neg_hi:[1,0,0]
	v_pk_fma_f16 v9, v5, v140, v141 op_sel:[0,1,1] op_sel_hi:[1,1,1] neg_lo:[1,0,0] neg_hi:[1,0,0]
	v_mfma_f32_16x16x32_f16 v[18:21], v[10:13], v[2:5], 0
	v_pk_fma_f16 v2, v88, v6, v2
	v_pk_fma_f16 v3, v89, v7, v3
	v_pk_fma_f16 v4, v90, v8, v4
	v_pk_fma_f16 v5, v91, v9, v5
	v_cndmask_b32_e64 v27, v27, v23, s[64:65]
	v_pk_fma_f16 v6, v2, v142, v143 op_sel:[0,1,1] op_sel_hi:[1,1,1] neg_lo:[1,0,0] neg_hi:[1,0,0]
	v_pk_fma_f16 v7, v3, v142, v143 op_sel:[0,1,1] op_sel_hi:[1,1,1] neg_lo:[1,0,0] neg_hi:[1,0,0]
	v_pk_fma_f16 v8, v4, v142, v143 op_sel:[0,1,1] op_sel_hi:[1,1,1] neg_lo:[1,0,0] neg_hi:[1,0,0]
	v_pk_fma_f16 v9, v5, v142, v143 op_sel:[0,1,1] op_sel_hi:[1,1,1] neg_lo:[1,0,0] neg_hi:[1,0,0]
	v_mfma_f32_16x16x32_f16 v[22:25], v[10:13], v[2:5], 0
	v_pk_fma_f16 v2, v92, v6, v2
	v_pk_fma_f16 v3, v93, v7, v3
	v_pk_fma_f16 v4, v94, v8, v4
	v_pk_fma_f16 v5, v95, v9, v5
	v_cndmask_b32_e64 v28, v28, v20, s[64:65]
	v_pk_fma_f16 v6, v2, v144, v145 op_sel:[0,1,1] op_sel_hi:[1,1,1] neg_lo:[1,0,0] neg_hi:[1,0,0]
	v_pk_fma_f16 v7, v3, v144, v145 op_sel:[0,1,1] op_sel_hi:[1,1,1] neg_lo:[1,0,0] neg_hi:[1,0,0]
	v_pk_fma_f16 v8, v4, v144, v145 op_sel:[0,1,1] op_sel_hi:[1,1,1] neg_lo:[1,0,0] neg_hi:[1,0,0]
	v_pk_fma_f16 v9, v5, v144, v145 op_sel:[0,1,1] op_sel_hi:[1,1,1] neg_lo:[1,0,0] neg_hi:[1,0,0]
	v_mfma_f32_16x16x32_f16 v[18:21], v[10:13], v[2:5], 0
	v_pk_fma_f16 v2, v96, v6, v2
	v_pk_fma_f16 v3, v97, v7, v3
	v_pk_fma_f16 v4, v98, v8, v4
	v_pk_fma_f16 v5, v99, v9, v5
	v_cndmask_b32_e64 v29, v29, v25, s[64:65]
	s_cmp_eq_u32 s72, 1
	s_cbranch_scc0 .Lc1_nsa0
	s_waitcnt lgkmcnt(1)
	v_readfirstlane_b32 s4, v45
	s_cmp_eq_u32 s4, 4
	s_cbranch_scc0 .Lc1_dslowa0

.Lc1_nsa0:
	v_pk_fma_f16 v6, v2, v146, v147 op_sel:[0,1,1] op_sel_hi:[1,1,1] neg_lo:[1,0,0] neg_hi:[1,0,0]
	v_pk_fma_f16 v7, v3, v146, v147 op_sel:[0,1,1] op_sel_hi:[1,1,1] neg_lo:[1,0,0] neg_hi:[1,0,0]
	v_pk_fma_f16 v8, v4, v146, v147 op_sel:[0,1,1] op_sel_hi:[1,1,1] neg_lo:[1,0,0] neg_hi:[1,0,0]
	v_pk_fma_f16 v9, v5, v146, v147 op_sel:[0,1,1] op_sel_hi:[1,1,1] neg_lo:[1,0,0] neg_hi:[1,0,0]
	v_mfma_f32_16x16x32_f16 v[22:25], v[10:13], v[2:5], 0
	v_pk_fma_f16 v2, v100, v6, v2
	v_pk_fma_f16 v3, v101, v7, v3
	v_pk_fma_f16 v4, v102, v8, v4
	v_pk_fma_f16 v5, v103, v9, v5
	v_cndmask_b32_e64 v26, v26, v18, s[66:67]
	v_pk_fma_f16 v6, v2, v148, v149 op_sel:[0,1,1] op_sel_hi:[1,1,1] neg_lo:[1,0,0] neg_hi:[1,0,0]
	v_pk_fma_f16 v7, v3, v148, v149 op_sel:[0,1,1] op_sel_hi:[1,1,1] neg_lo:[1,0,0] neg_hi:[1,0,0]
	v_pk_fma_f16 v8, v4, v148, v149 op_sel:[0,1,1] op_sel_hi:[1,1,1] neg_lo:[1,0,0] neg_hi:[1,0,0]
	v_pk_fma_f16 v9, v5, v148, v149 op_sel:[0,1,1] op_sel_hi:[1,1,1] neg_lo:[1,0,0] neg_hi:[1,0,0]
	v_mfma_f32_16x16x32_f16 v[18:21], v[10:13], v[2:5], 0
	v_pk_fma_f16 v2, v104, v6, v2
	v_pk_fma_f16 v3, v105, v7, v3
	v_pk_fma_f16 v4, v106, v8, v4
	v_pk_fma_f16 v5, v107, v9, v5
	v_cndmask_b32_e64 v27, v27, v23, s[66:67]
	v_pk_fma_f16 v6, v2, v150, v151 op_sel:[0,1,1] op_sel_hi:[1,1,1] neg_lo:[1,0,0] neg_hi:[1,0,0]
	v_pk_fma_f16 v7, v3, v150, v151 op_sel:[0,1,1] op_sel_hi:[1,1,1] neg_lo:[1,0,0] neg_hi:[1,0,0]
	v_pk_fma_f16 v8, v4, v150, v151 op_sel:[0,1,1] op_sel_hi:[1,1,1] neg_lo:[1,0,0] neg_hi:[1,0,0]
	v_pk_fma_f16 v9, v5, v150, v151 op_sel:[0,1,1] op_sel_hi:[1,1,1] neg_lo:[1,0,0] neg_hi:[1,0,0]
	v_mfma_f32_16x16x32_f16 v[22:25], v[10:13], v[2:5], 0
	v_pk_fma_f16 v2, v108, v6, v2
	v_pk_fma_f16 v3, v109, v7, v3
	v_pk_fma_f16 v4, v110, v8, v4
	v_pk_fma_f16 v5, v111, v9, v5
	v_cndmask_b32_e64 v28, v28, v20, s[66:67]

.Lc1_dgoa0:
	ds_read_b128 v[112:115], v43 offset:0
	ds_read_b128 v[116:119], v43 offset:1024
	s_waitcnt lgkmcnt(0)
	s_branch .Lc1_dbacka0
.Lc1_alt1:
	s_mov_b32 s72, 0
	s_cmp_eq_u32 s36, s71
	s_cbranch_scc0 .Lc1_nda1
	s_mov_b32 s72, 1
	ds_read_b32 v45, v36 offset:128
	ds_read_b128 v[112:115], v43 offset:2048
	ds_read_b128 v[116:119], v43 offset:3072
.Lc1_nda1:
	v_pk_fma_f16 v6, v2, v138, v139 op_sel:[0,1,1] op_sel_hi:[1,1,1] neg_lo:[1,0,0] neg_hi:[1,0,0]
	v_pk_fma_f16 v7, v3, v138, v139 op_sel:[0,1,1] op_sel_hi:[1,1,1] neg_lo:[1,0,0] neg_hi:[1,0,0]
	v_pk_fma_f16 v8, v4, v138, v139 op_sel:[0,1,1] op_sel_hi:[1,1,1] neg_lo:[1,0,0] neg_hi:[1,0,0]
	v_pk_fma_f16 v9, v5, v138, v139 op_sel:[0,1,1] op_sel_hi:[1,1,1] neg_lo:[1,0,0] neg_hi:[1,0,0]
	v_mfma_f32_16x16x32_f16 v[22:25], v[14:17], v[2:5], 0
	ds_read2_b64 v[108:111], v32 offset0:31 offset1:233
	v_pk_fma_f16 v2, v84, v6, v2
	v_pk_fma_f16 v3, v85, v7, v3
	v_pk_fma_f16 v4, v86, v8, v4
	v_pk_fma_f16 v5, v87, v9, v5
	v_cndmask_b32_e64 v26, v26, v18, s[64:65]
	s_waitcnt lgkmcnt(0)
	v_pk_fma_f16 v6, v2, v140, v141 op_sel:[0,1,1] op_sel_hi:[1,1,1] neg_lo:[1,0,0] neg_hi:[1,0,0]
	v_pk_fma_f16 v7, v3, v140, v141 op_sel:[0,1,1] op_sel_hi:[1,1,1] neg_lo:[1,0,0] neg_hi:[1,0,0]
	v_pk_fma_f16 v8, v4, v140, v141 op_sel:[0,1,1] op_sel_hi:[1,1,1] neg_lo:[1,0,0] neg_hi:[1,0,0]
	v_pk_fma_f16 v9, v5, v140, v141 op_sel:[0,1,1] op_sel_hi:[1,1,1] neg_lo:[1,0,0] neg_hi:[1,0,0]
	v_mfma_f32_16x16x32_f16 v[18:21], v[14:17], v[2:5], 0
	v_pk_fma_f16 v2, v88, v6, v2
	v_pk_fma_f16 v3, v89, v7, v3
	v_pk_fma_f16 v4, v90, v8, v4
	v_pk_fma_f16 v5, v91, v9, v5
	v_cndmask_b32_e64 v27, v27, v23, s[64:65]
	v_pk_fma_f16 v6, v2, v142, v143 op_sel:[0,1,1] op_sel_hi:[1,1,1] neg_lo:[1,0,0] neg_hi:[1,0,0]
	v_pk_fma_f16 v7, v3, v142, v143 op_sel:[0,1,1] op_sel_hi:[1,1,1] neg_lo:[1,0,0] neg_hi:[1,0,0]
	v_pk_fma_f16 v8, v4, v142, v143 op_sel:[0,1,1] op_sel_hi:[1,1,1] neg_lo:[1,0,0] neg_hi:[1,0,0]
	v_pk_fma_f16 v9, v5, v142, v143 op_sel:[0,1,1] op_sel_hi:[1,1,1] neg_lo:[1,0,0] neg_hi:[1,0,0]
	v_mfma_f32_16x16x32_f16 v[22:25], v[14:17], v[2:5], 0
	v_pk_fma_f16 v2, v92, v6, v2
	v_pk_fma_f16 v3, v93, v7, v3
	v_pk_fma_f16 v4, v94, v8, v4
	v_pk_fma_f16 v5, v95, v9, v5
	v_cndmask_b32_e64 v28, v28, v20, s[64:65]
	v_pk_fma_f16 v6, v2, v144, v145 op_sel:[0,1,1] op_sel_hi:[1,1,1] neg_lo:[1,0,0] neg_hi:[1,0,0]
	v_pk_fma_f16 v7, v3, v144, v145 op_sel:[0,1,1] op_sel_hi:[1,1,1] neg_lo:[1,0,0] neg_hi:[1,0,0]
	v_pk_fma_f16 v8, v4, v144, v145 op_sel:[0,1,1] op_sel_hi:[1,1,1] neg_lo:[1,0,0] neg_hi:[1,0,0]
	v_pk_fma_f16 v9, v5, v144, v145 op_sel:[0,1,1] op_sel_hi:[1,1,1] neg_lo:[1,0,0] neg_hi:[1,0,0]
	v_mfma_f32_16x16x32_f16 v[18:21], v[14:17], v[2:5], 0
	v_pk_fma_f16 v2, v96, v6, v2
	v_pk_fma_f16 v3, v97, v7, v3
	v_pk_fma_f16 v4, v98, v8, v4
	v_pk_fma_f16 v5, v99, v9, v5
	v_cndmask_b32_e64 v29, v29, v25, s[64:65]
	s_cmp_eq_u32 s72, 1
	s_cbranch_scc0 .Lc1_nsa1
	s_waitcnt lgkmcnt(1)
	v_readfirstlane_b32 s4, v45
	s_cmp_eq_u32 s4, 4
	s_cbranch_scc0 .Lc1_dslowa1

.Lc1_nsa1:
	v_pk_fma_f16 v6, v2, v146, v147 op_sel:[0,1,1] op_sel_hi:[1,1,1] neg_lo:[1,0,0] neg_hi:[1,0,0]
	v_pk_fma_f16 v7, v3, v146, v147 op_sel:[0,1,1] op_sel_hi:[1,1,1] neg_lo:[1,0,0] neg_hi:[1,0,0]
	v_pk_fma_f16 v8, v4, v146, v147 op_sel:[0,1,1] op_sel_hi:[1,1,1] neg_lo:[1,0,0] neg_hi:[1,0,0]
	v_pk_fma_f16 v9, v5, v146, v147 op_sel:[0,1,1] op_sel_hi:[1,1,1] neg_lo:[1,0,0] neg_hi:[1,0,0]
	v_mfma_f32_16x16x32_f16 v[22:25], v[14:17], v[2:5], 0
	v_pk_fma_f16 v2, v100, v6, v2
	v_pk_fma_f16 v3, v101, v7, v3
	v_pk_fma_f16 v4, v102, v8, v4
	v_pk_fma_f16 v5, v103, v9, v5
	v_cndmask_b32_e64 v26, v26, v18, s[66:67]
	v_pk_fma_f16 v6, v2, v148, v149 op_sel:[0,1,1] op_sel_hi:[1,1,1] neg_lo:[1,0,0] neg_hi:[1,0,0]
	v_pk_fma_f16 v7, v3, v148, v149 op_sel:[0,1,1] op_sel_hi:[1,1,1] neg_lo:[1,0,0] neg_hi:[1,0,0]
	v_pk_fma_f16 v8, v4, v148, v149 op_sel:[0,1,1] op_sel_hi:[1,1,1] neg_lo:[1,0,0] neg_hi:[1,0,0]
	v_pk_fma_f16 v9, v5, v148, v149 op_sel:[0,1,1] op_sel_hi:[1,1,1] neg_lo:[1,0,0] neg_hi:[1,0,0]
	v_mfma_f32_16x16x32_f16 v[18:21], v[14:17], v[2:5], 0
	v_pk_fma_f16 v2, v104, v6, v2
	v_pk_fma_f16 v3, v105, v7, v3
	v_pk_fma_f16 v4, v106, v8, v4
	v_pk_fma_f16 v5, v107, v9, v5
	v_cndmask_b32_e64 v27, v27, v23, s[66:67]
	v_pk_fma_f16 v6, v2, v150, v151 op_sel:[0,1,1] op_sel_hi:[1,1,1] neg_lo:[1,0,0] neg_hi:[1,0,0]
	v_pk_fma_f16 v7, v3, v150, v151 op_sel:[0,1,1] op_sel_hi:[1,1,1] neg_lo:[1,0,0] neg_hi:[1,0,0]
	v_pk_fma_f16 v8, v4, v150, v151 op_sel:[0,1,1] op_sel_hi:[1,1,1] neg_lo:[1,0,0] neg_hi:[1,0,0]
	v_pk_fma_f16 v9, v5, v150, v151 op_sel:[0,1,1] op_sel_hi:[1,1,1] neg_lo:[1,0,0] neg_hi:[1,0,0]
	v_mfma_f32_16x16x32_f16 v[22:25], v[14:17], v[2:5], 0
	v_pk_fma_f16 v2, v108, v6, v2
	v_pk_fma_f16 v3, v109, v7, v3
	v_pk_fma_f16 v4, v110, v8, v4
	v_pk_fma_f16 v5, v111, v9, v5
	v_cndmask_b32_e64 v28, v28, v20, s[66:67]

.Lc1_dgoa1:
	ds_read_b128 v[112:115], v43 offset:2048
	ds_read_b128 v[116:119], v43 offset:3072
	s_waitcnt lgkmcnt(0)
	s_branch .Lc1_dbacka1
.LBB0_107:
	global_load_dwordx4 v[66:69], v[182:183], off offset:256
	global_load_dwordx4 v[70:73], v[182:183], off offset:320
	global_load_dwordx4 v[74:77], v[182:183], off offset:384
	global_load_dwordx4 v[78:81], v[182:183], off offset:448
	s_cmp_gt_u32 s39, 10
	s_cbranch_scc1 .LBB0_75
